# wait for all write-through stores (s_waitcnt vmcnt(0)) before every s_endpgm so sc1 data is complete at the kernel boundary
# speedup vs baseline: 1.0312x; 1.0142x over previous
.LBB0_9:
	s_ashr_i32 s9, s8, 31
	s_lshl_b64 s[10:11], s[8:9], 14
	s_waitcnt lgkmcnt(0)
	s_add_u32 s4, s4, s10
	s_addc_u32 s5, s5, s11
	v_and_b32_e32 v1, 31, v0
	v_bfe_u32 v18, v0, 5, 1
	v_and_b32_e32 v19, 0xc0, v0
	v_lshl_or_b32 v28, v1, 1, v18
	v_add_lshl_u32 v28, v28, v19, 4
	global_load_dwordx4 v[2:5], v28, s[4:5] nt
	s_add_u32 s4, s4, 0x1000
	s_addc_u32 s5, s5, 0
	global_load_dwordx4 v[6:9], v28, s[4:5] nt
	s_add_u32 s4, s4, 0x1000
	s_addc_u32 s5, s5, 0
	global_load_dwordx4 v[10:13], v28, s[4:5] nt
	s_add_u32 s4, s4, 0x1000
	s_addc_u32 s5, s5, 0
	global_load_dwordx4 v[14:17], v28, s[4:5] nt
	s_lshl_b64 s[10:11], s[8:9], 13
	s_add_u32 s6, s6, s10
	s_addc_u32 s7, s7, s11
	v_lshlrev_b32_e32 v29, 4, v1
	v_lshl_or_b32 v29, v19, 3, v29
	v_lshl_or_b32 v29, v18, 11, v29
	v_add_u32_e32 v28, 0x1000, v29
	s_waitcnt vmcnt(2)
	v_cvt_pk_f16_f32 v20, v2, v3
	v_cvt_pk_f16_f32 v21, v4, v5
	v_cvt_pk_f16_f32 v22, v6, v7
	v_cvt_pk_f16_f32 v23, v8, v9
	s_nop 1
	v_permlane32_swap_b32_e32 v20, v22
	v_permlane32_swap_b32_e32 v21, v23
	global_store_dwordx4 v29, v[20:23], s[6:7] sc1
	s_waitcnt vmcnt(1)
	v_cvt_pk_f16_f32 v24, v10, v11
	v_cvt_pk_f16_f32 v25, v12, v13
	v_cvt_pk_f16_f32 v26, v14, v15
	v_cvt_pk_f16_f32 v27, v16, v17
	s_nop 1
	v_permlane32_swap_b32_e32 v24, v26
	v_permlane32_swap_b32_e32 v25, v27
	global_store_dwordx4 v28, v[24:27], s[6:7] sc1
	s_mov_b64 s[4:5], 0

.LBB0_16:
	s_waitcnt vmcnt(0)
	s_endpgm

	.amdhsa_kernel _Z8cvt3_f16PKfPDF16_iS0_S1_iS0_S1_iPfS2_
		.amdhsa_group_segment_fixed_size 0
		.amdhsa_private_segment_fixed_size 0
		.amdhsa_kernarg_size 88
		.amdhsa_user_sgpr_count 2
		.amdhsa_user_sgpr_dispatch_ptr 0
		.amdhsa_user_sgpr_queue_ptr 0
		.amdhsa_user_sgpr_kernarg_segment_ptr 1
		.amdhsa_user_sgpr_dispatch_id 0
		.amdhsa_user_sgpr_kernarg_preload_length 0
		.amdhsa_user_sgpr_kernarg_preload_offset 0
		.amdhsa_user_sgpr_private_segment_size 0
		.amdhsa_uses_dynamic_stack 0
		.amdhsa_enable_private_segment 0
		.amdhsa_system_sgpr_workgroup_id_x 1
		.amdhsa_system_sgpr_workgroup_id_y 0
		.amdhsa_system_sgpr_workgroup_id_z 0
		.amdhsa_system_sgpr_workgroup_info 0
		.amdhsa_system_vgpr_workitem_id 0
		.amdhsa_next_free_vgpr 30
		.amdhsa_next_free_sgpr 12
		.amdhsa_accum_offset 32
		.amdhsa_reserve_vcc 1
		.amdhsa_float_round_mode_32 0
		.amdhsa_float_round_mode_16_64 0
		.amdhsa_float_denorm_mode_32 3
		.amdhsa_float_denorm_mode_16_64 3
		.amdhsa_dx10_clamp 1
		.amdhsa_ieee_mode 1
		.amdhsa_fp16_overflow 0
		.amdhsa_tg_split 0
		.amdhsa_exception_fp_ieee_invalid_op 0
		.amdhsa_exception_fp_denorm_src 0
		.amdhsa_exception_fp_ieee_div_zero 0
		.amdhsa_exception_fp_ieee_overflow 0
		.amdhsa_exception_fp_ieee_underflow 0
		.amdhsa_exception_fp_ieee_inexact 0
		.amdhsa_exception_int_div_zero 0
	.end_amdhsa_kernel

.LBB1_12:
	s_lshl_b32 s2, s13, 7
	v_lshlrev_b32_e32 v64, 1, v64
	s_add_i32 s2, s2, s14
	v_lshl_or_b32 v64, s12, 8, v64
	v_lshl_or_b32 v66, v65, 2, s2
	v_or_b32_e32 v64, s15, v64
	v_ashrrev_i32_e32 v65, 31, v64
	v_ashrrev_i32_e32 v67, 31, v66
	s_waitcnt lgkmcnt(0)
	v_lshl_add_u64 v[64:65], v[64:65], 2, s[0:1]
	v_lshlrev_b64 v[70:71], 13, v[66:67]
	v_mov_b32_e32 v68, v60
	v_mov_b32_e32 v69, v56
	v_lshl_add_u64 v[70:71], v[64:65], 0, v[70:71]
	v_or_b32_e32 v60, 1, v66
	global_store_dwordx2 v[70:71], v[68:69], off nt
	v_mov_b32_e32 v56, v61
	v_ashrrev_i32_e32 v61, 31, v60
	v_or_b32_e32 v68, 2, v66
	v_lshlrev_b64 v[60:61], 13, v[60:61]
	v_ashrrev_i32_e32 v69, 31, v68
	v_lshl_add_u64 v[60:61], v[64:65], 0, v[60:61]
	v_lshlrev_b64 v[68:69], 13, v[68:69]
	global_store_dwordx2 v[60:61], v[56:57], off nt
	v_mov_b32_e32 v56, v62
	v_mov_b32_e32 v57, v58
	v_lshl_add_u64 v[68:69], v[64:65], 0, v[68:69]
	global_store_dwordx2 v[68:69], v[56:57], off nt
	v_or_b32_e32 v56, 3, v66
	v_ashrrev_i32_e32 v57, 31, v56
	v_lshlrev_b64 v[56:57], 13, v[56:57]
	v_mov_b32_e32 v58, v63
	v_lshl_add_u64 v[56:57], v[64:65], 0, v[56:57]
	global_store_dwordx2 v[56:57], v[58:59], off nt
	v_or_b32_e32 v58, 16, v66
	v_ashrrev_i32_e32 v59, 31, v58
	v_lshlrev_b64 v[58:59], 13, v[58:59]
	v_mov_b32_e32 v62, v52
	v_mov_b32_e32 v63, v48
	v_lshl_add_u64 v[58:59], v[64:65], 0, v[58:59]
	v_or_b32_e32 v52, 17, v66
	global_store_dwordx2 v[58:59], v[62:63], off nt
	v_mov_b32_e32 v48, v53
	v_ashrrev_i32_e32 v53, 31, v52
	v_or_b32_e32 v62, 18, v66
	v_lshlrev_b64 v[52:53], 13, v[52:53]
	v_ashrrev_i32_e32 v63, 31, v62
	v_lshl_add_u64 v[52:53], v[64:65], 0, v[52:53]
	v_lshlrev_b64 v[62:63], 13, v[62:63]
	global_store_dwordx2 v[52:53], v[48:49], off nt
	v_mov_b32_e32 v48, v54
	v_mov_b32_e32 v49, v50
	v_lshl_add_u64 v[62:63], v[64:65], 0, v[62:63]
	global_store_dwordx2 v[62:63], v[48:49], off nt
	v_or_b32_e32 v48, 19, v66
	v_ashrrev_i32_e32 v49, 31, v48
	v_lshlrev_b64 v[48:49], 13, v[48:49]
	v_mov_b32_e32 v50, v55
	v_lshl_add_u64 v[48:49], v[64:65], 0, v[48:49]
	global_store_dwordx2 v[48:49], v[50:51], off nt
	v_or_b32_e32 v50, 32, v66
	v_ashrrev_i32_e32 v51, 31, v50
	v_lshlrev_b64 v[50:51], 13, v[50:51]
	v_mov_b32_e32 v54, v44
	v_mov_b32_e32 v55, v40
	v_lshl_add_u64 v[50:51], v[64:65], 0, v[50:51]
	v_or_b32_e32 v44, 33, v66
	global_store_dwordx2 v[50:51], v[54:55], off nt
	v_mov_b32_e32 v40, v45
	v_ashrrev_i32_e32 v45, 31, v44
	v_or_b32_e32 v54, 34, v66
	v_lshlrev_b64 v[44:45], 13, v[44:45]
	v_ashrrev_i32_e32 v55, 31, v54
	v_lshl_add_u64 v[44:45], v[64:65], 0, v[44:45]
	v_lshlrev_b64 v[54:55], 13, v[54:55]
	global_store_dwordx2 v[44:45], v[40:41], off nt
	v_mov_b32_e32 v40, v46
	v_mov_b32_e32 v41, v42
	v_lshl_add_u64 v[54:55], v[64:65], 0, v[54:55]
	global_store_dwordx2 v[54:55], v[40:41], off nt
	v_or_b32_e32 v40, 35, v66
	v_ashrrev_i32_e32 v41, 31, v40
	v_lshlrev_b64 v[40:41], 13, v[40:41]
	v_mov_b32_e32 v42, v47
	v_lshl_add_u64 v[40:41], v[64:65], 0, v[40:41]
	global_store_dwordx2 v[40:41], v[42:43], off nt
	v_or_b32_e32 v42, 48, v66
	v_ashrrev_i32_e32 v43, 31, v42
	v_lshlrev_b64 v[42:43], 13, v[42:43]
	v_mov_b32_e32 v46, v36
	v_mov_b32_e32 v47, v32
	v_lshl_add_u64 v[42:43], v[64:65], 0, v[42:43]
	v_or_b32_e32 v36, 49, v66
	global_store_dwordx2 v[42:43], v[46:47], off nt
	v_mov_b32_e32 v32, v37
	v_ashrrev_i32_e32 v37, 31, v36
	v_or_b32_e32 v46, 50, v66
	v_lshlrev_b64 v[36:37], 13, v[36:37]
	v_ashrrev_i32_e32 v47, 31, v46
	v_lshl_add_u64 v[36:37], v[64:65], 0, v[36:37]
	v_lshlrev_b64 v[46:47], 13, v[46:47]
	global_store_dwordx2 v[36:37], v[32:33], off nt
	v_mov_b32_e32 v32, v38
	v_mov_b32_e32 v33, v34
	v_lshl_add_u64 v[46:47], v[64:65], 0, v[46:47]
	global_store_dwordx2 v[46:47], v[32:33], off nt
	v_or_b32_e32 v32, 51, v66
	v_ashrrev_i32_e32 v33, 31, v32
	v_lshlrev_b64 v[32:33], 13, v[32:33]
	v_mov_b32_e32 v34, v39
	v_lshl_add_u64 v[32:33], v[64:65], 0, v[32:33]
	global_store_dwordx2 v[32:33], v[34:35], off nt
	v_mov_b32_e32 v34, v24
	v_mov_b32_e32 v35, v28
	v_mov_b32_e32 v28, v25
	v_mov_b32_e32 v24, v26
	v_mov_b32_e32 v25, v30
	global_store_dwordx2 v[68:69], v[24:25], off offset:512 nt
	v_mov_b32_e32 v24, v16
	v_mov_b32_e32 v25, v20
	v_mov_b32_e32 v20, v17
	v_mov_b32_e32 v16, v18
	v_mov_b32_e32 v17, v22
	global_store_dwordx2 v[62:63], v[16:17], off offset:512 nt
	v_mov_b32_e32 v16, v8
	v_mov_b32_e32 v17, v12
	v_mov_b32_e32 v12, v9
	v_mov_b32_e32 v8, v10
	v_mov_b32_e32 v9, v14
	v_mov_b32_e32 v30, v27
	v_mov_b32_e32 v22, v19
	global_store_dwordx2 v[54:55], v[8:9], off offset:512 nt
	v_mov_b32_e32 v14, v11
	v_mov_b32_e32 v8, v0
	v_mov_b32_e32 v9, v4
	v_mov_b32_e32 v4, v1
	v_mov_b32_e32 v0, v2
	v_mov_b32_e32 v1, v6
	v_mov_b32_e32 v6, v3
	global_store_dwordx2 v[70:71], v[34:35], off offset:512 nt
	global_store_dwordx2 v[60:61], v[28:29], off offset:512 nt
	global_store_dwordx2 v[56:57], v[30:31], off offset:512 nt
	global_store_dwordx2 v[58:59], v[24:25], off offset:512 nt
	global_store_dwordx2 v[52:53], v[20:21], off offset:512 nt
	global_store_dwordx2 v[48:49], v[22:23], off offset:512 nt
	global_store_dwordx2 v[50:51], v[16:17], off offset:512 nt
	global_store_dwordx2 v[44:45], v[12:13], off offset:512 nt
	global_store_dwordx2 v[40:41], v[14:15], off offset:512 nt
	global_store_dwordx2 v[42:43], v[8:9], off offset:512 nt
	global_store_dwordx2 v[36:37], v[4:5], off offset:512 nt
	global_store_dwordx2 v[46:47], v[0:1], off offset:512 nt
	global_store_dwordx2 v[32:33], v[6:7], off offset:512 nt
	s_waitcnt vmcnt(0)
	s_endpgm

_Z8gemm_qkvPKDF16_S0_7EpiArgs:
	s_load_dwordx4 s[4:7], s[0:1], 0x0
	s_lshr_b32 s3, s2, 8
	s_and_b32 s10, s2, 31
	s_lshr_b32 s11, s2, 1
	s_and_b32 s11, s11, 0x60
	s_or_b32 s10, s10, s11
	s_and_b32 s11, s2, 0x7f
	s_cmp_eq_u32 s3, 0
	s_cselect_b32 s10, s10, s11
	s_cselect_b32 s11, 5, 7
	s_lshr_b32 s11, s2, s11
	s_and_b32 s11, s11, 1
	s_and_b32 s2, s10, 31
	s_lshl_b32 s3, s3, 5
	s_or_b32 s2, s2, s3
	s_and_b32 s10, s10, 0x60
	s_lshl_b32 s10, s10, 1
	s_or_b32 s2, s2, s10
	s_lshl_b32 s11, s11, 8
	s_or_b32 s2, s2, s11
	s_cmpk_gt_u32 s2, 0xff
	s_waitcnt lgkmcnt(0)
	s_mov_b64 s[8:9], s[6:7]
	s_mov_b64 s[6:7], -1
	s_cbranch_scc1 .LBB2_3
	s_and_b64 vcc, exec, s[6:7]
	s_cbranch_vccnz .LBB2_16

.LBB2_24:
	s_or_b64 exec, exec, s[0:1]
	s_and_b32 s4, s20, 0x700000
	s_cmp_lt_u32 s3, 64
	s_cselect_b64 vcc, -1, 0
	s_and_b64 s[0:1], vcc, exec
	s_cselect_b32 s1, s13, s15
	s_cselect_b32 s0, s12, s14
	s_lshl_b32 s3, s4, 1
	v_mov_b32_e32 v137, 0x3e0293ee
	s_add_u32 s0, s0, s3
	v_cndmask_b32_e32 v158, 1.0, v137, vcc
	s_addc_u32 s1, s1, 0
	v_lshlrev_b32_e32 v136, 6, v136
	v_lshlrev_b32_e32 v137, 2, v130
	v_lshlrev_b32_e32 v130, 4, v130
	v_add3_u32 v162, 0, v136, v137
	v_add_u32_e32 v182, 0, v130
	v_lshl_add_u64 v[136:137], s[0:1], 0, v[130:131]
	v_lshrrev_b16_e32 v130, 2, v0
	v_lshlrev_b16_e32 v192, 6, v154
	v_and_b32_e32 v191, 12, v130
	v_bitop3_b16 v194, v192, v130, 12 bitop3:0xf8
	v_lshlrev_b32_e32 v130, 2, v187
	v_lshlrev_b32_e32 v189, 2, v189
	v_lshlrev_b32_e32 v188, 2, v188
	v_or_b32_e32 v154, v130, v1
	v_bitop3_b32 v130, v130, 1, v1 bitop3:0x36
	v_lshlrev_b32_e32 v190, 2, v190
	v_or_b32_e32 v195, v189, v1
	v_or_b32_e32 v196, v188, v1
	v_lshl_add_u32 v154, v154, 2, 0
	v_lshl_add_u32 v130, v130, 2, 0
	v_or_b32_e32 v193, v190, v1
	v_bitop3_b32 v190, v190, 1, v1 bitop3:0x36
	v_lshl_add_u32 v195, v195, 2, 0
	v_bitop3_b32 v189, v189, 1, v1 bitop3:0x36
	v_lshl_add_u32 v196, v196, 2, 0
	v_bitop3_b32 v188, v188, 1, v1 bitop3:0x36
	s_waitcnt lgkmcnt(0)
	s_barrier
	v_lshl_add_u32 v193, v193, 2, 0
	v_lshl_add_u32 v190, v190, 2, 0
	v_lshl_add_u32 v189, v189, 2, 0
	v_lshl_add_u32 v188, v188, 2, 0
	ds_read_b32 v154, v154
	ds_read_b32 v130, v130
	ds_read_b32 v197, v193
	ds_read_b32 v198, v190
	ds_read_b32 v195, v195
	ds_read_b32 v199, v189
	ds_read_b32 v196, v196
	ds_read_b32 v200, v188
	s_waitcnt lgkmcnt(6)
	v_add_f32_e32 v130, v154, v130
	v_bfrev_b32_e32 v154, 44
	v_fmamk_f32 v130, v130, 0x3c000000, v154
	v_rsq_f32_e32 v188, v130
	v_bitop3_b16 v201, v192, 16, v191 bitop3:0xfe
	v_bitop3_b16 v202, v192, 32, v191 bitop3:0xfe
	v_bitop3_b16 v130, v192, 48, v191 bitop3:0xfe
	v_mul_f32_e32 v188, v158, v188
	v_mov_b32_e32 v190, v118
	v_mov_b32_e32 v191, v114
	v_mov_b32_e32 v192, v122
	v_mov_b32_e32 v193, v126
	v_pk_mul_f32 v[190:191], v[190:191], v[188:189] op_sel_hi:[1,0]
	v_pk_mul_f32 v[188:189], v[192:193], v[188:189] op_sel_hi:[1,0]
	v_and_b32_e32 v161, 0x80, v0
	s_movk_i32 s1, 0x4c
	s_waitcnt vmcnt(6)
	v_pk_mul_f32 v[192:193], v[144:145], v[188:189]
	s_movk_i32 s0, 0x110
	v_and_or_b32 v187, v187, s1, v161
	v_pk_fma_f32 v[192:193], v[142:143], v[190:191], v[192:193]
	v_pk_mul_f32 v[190:191], v[144:145], v[190:191]
	v_mad_u32_u24 v187, v187, s0, v162
	v_pk_fma_f32 v[188:189], v[142:143], v[188:189], v[190:191] neg_lo:[0,0,1] neg_hi:[0,0,1]
	v_cvt_pk_f16_f32 v114, v192, v193
	v_cvt_pk_f16_f32 v122, v188, v189
	v_add_u32_e32 v118, 0x1000, v187
	ds_write2_b32 v118, v114, v122 offset1:32
	s_waitcnt lgkmcnt(5)
	v_add_f32_e32 v114, v197, v198
	v_fmamk_f32 v114, v114, 0x3c000000, v154
	v_rsq_f32_e32 v114, v114
	s_waitcnt vmcnt(4)
	v_pk_mul_f32 v[190:191], v[142:143], v[134:135]
	v_mov_b32_e32 v126, v123
	v_pk_mul_f32 v[188:189], v[144:145], v[134:135]
	v_mul_f32_e32 v122, v158, v114
	v_or_b32_sdwa v114, v161, v194 dst_sel:DWORD dst_unused:UNUSED_PAD src0_sel:DWORD src1_sel:WORD_0
	v_mad_u32_u24 v187, v114, s0, v162
	v_mov_b32_e32 v114, v119
	v_pk_fma_f32 v[190:191], v[144:145], v[132:133], v[190:191]
	v_pk_mul_f32 v[114:115], v[114:115], v[122:123] op_sel_hi:[1,0]
	v_pk_mul_f32 v[122:123], v[126:127], v[122:123] op_sel_hi:[1,0]
	v_pk_fma_f32 v[188:189], v[142:143], v[132:133], v[188:189] neg_lo:[0,0,1] neg_hi:[0,0,1]
	v_pk_mul_f32 v[126:127], v[190:191], v[122:123]
	v_mov_b32_e32 v192, v124
	v_pk_fma_f32 v[126:127], v[188:189], v[114:115], v[126:127]
	v_pk_mul_f32 v[114:115], v[190:191], v[114:115]
	v_cvt_pk_f16_f32 v119, v126, v127
	v_pk_fma_f32 v[114:115], v[188:189], v[122:123], v[114:115] neg_lo:[0,0,1] neg_hi:[0,0,1]
	v_pk_mul_f32 v[122:123], v[134:135], v[190:191]
	v_cvt_pk_f16_f32 v115, v114, v115
	v_add_u32_e32 v114, 0x1000, v187
	ds_write2_b32 v114, v119, v115 offset0:68 offset1:100
	s_waitcnt lgkmcnt(4)
	v_add_f32_e32 v115, v195, v199
	v_fmamk_f32 v115, v115, 0x3c000000, v154
	v_rsq_f32_e32 v115, v115
	v_pk_mul_f32 v[126:127], v[132:133], v[190:191]
	v_pk_fma_f32 v[122:123], v[132:133], v[188:189], v[122:123] neg_lo:[0,0,1] neg_hi:[0,0,1]
	v_pk_fma_f32 v[126:127], v[134:135], v[188:189], v[126:127]
	v_mul_f32_e32 v188, v158, v115
	v_mov_b32_e32 v190, v120
	v_mov_b32_e32 v191, v116
	v_mov_b32_e32 v193, v128
	v_pk_mul_f32 v[190:191], v[190:191], v[188:189] op_sel_hi:[1,0]
	v_pk_mul_f32 v[188:189], v[192:193], v[188:189] op_sel_hi:[1,0]
	v_mov_b32_e32 v128, v125
	v_pk_mul_f32 v[192:193], v[126:127], v[188:189]
	s_movk_i32 s1, 0x5c
	v_pk_fma_f32 v[192:193], v[122:123], v[190:191], v[192:193]
	v_pk_mul_f32 v[190:191], v[126:127], v[190:191]
	v_cvt_pk_f16_f32 v115, v192, v193
	v_pk_fma_f32 v[188:189], v[122:123], v[188:189], v[190:191] neg_lo:[0,0,1] neg_hi:[0,0,1]
	s_movk_i32 s3, 0x6c
	v_cvt_pk_f16_f32 v116, v188, v189
	ds_write2_b32 v114, v115, v116 offset0:136 offset1:168
	s_waitcnt lgkmcnt(3)
	v_add_f32_e32 v115, v196, v200
	v_fmamk_f32 v115, v115, 0x3c000000, v154
	v_rsq_f32_e32 v115, v115
	v_pk_mul_f32 v[188:189], v[134:135], v[126:127]
	v_pk_mul_f32 v[126:127], v[132:133], v[126:127]
	v_mov_b32_e32 v116, v121
	v_mul_f32_e32 v120, v158, v115
	v_pk_fma_f32 v[188:189], v[132:133], v[122:123], v[188:189] neg_lo:[0,0,1] neg_hi:[0,0,1]
	v_pk_fma_f32 v[122:123], v[134:135], v[122:123], v[126:127]
	v_pk_mul_f32 v[116:117], v[116:117], v[120:121] op_sel_hi:[1,0]
	v_pk_mul_f32 v[120:121], v[128:129], v[120:121] op_sel_hi:[1,0]
	v_mov_b32_e32 v126, v106
	v_pk_mul_f32 v[124:125], v[122:123], v[120:121]
	v_mov_b32_e32 v127, v110
	v_pk_fma_f32 v[124:125], v[188:189], v[116:117], v[124:125]
	v_pk_mul_f32 v[116:117], v[122:123], v[116:117]
	v_cvt_pk_f16_f32 v115, v124, v125
	v_pk_fma_f32 v[116:117], v[188:189], v[120:121], v[116:117] neg_lo:[0,0,1] neg_hi:[0,0,1]
	v_lshlrev_b32_e32 v120, 2, v186
	v_cvt_pk_f16_f32 v116, v116, v117
	ds_write2_b32 v114, v115, v116 offset0:204 offset1:236
	v_lshlrev_b32_e32 v115, 2, v183
	v_or_b32_e32 v119, v115, v1
	v_bitop3_b32 v115, v115, 1, v1 bitop3:0x36
	v_lshlrev_b32_e32 v122, 2, v185
	v_lshlrev_b32_e32 v124, 2, v184
	v_lshl_add_u32 v119, v119, 2, 0
	v_lshl_add_u32 v115, v115, 2, 0
	v_or_b32_e32 v121, v120, v1
	v_bitop3_b32 v120, v120, 1, v1 bitop3:0x36
	v_or_b32_e32 v123, v122, v1
	v_bitop3_b32 v122, v122, 1, v1 bitop3:0x36
	v_or_b32_e32 v125, v124, v1
	v_bitop3_b32 v124, v124, 1, v1 bitop3:0x36
	v_lshl_add_u32 v121, v121, 2, 0
	v_lshl_add_u32 v120, v120, 2, 0
	v_lshl_add_u32 v123, v123, 2, 0
	v_lshl_add_u32 v122, v122, 2, 0
	v_lshl_add_u32 v125, v125, 2, 0
	v_lshl_add_u32 v124, v124, 2, 0
	ds_read_b32 v119, v119
	ds_read_b32 v115, v115
	ds_read_b32 v128, v121
	ds_read_b32 v129, v120
	ds_read_b32 v184, v123
	ds_read_b32 v185, v122
	ds_read_b32 v186, v125
	ds_read_b32 v187, v124
	s_waitcnt lgkmcnt(6)
	v_add_f32_e32 v115, v119, v115
	v_fmamk_f32 v115, v115, 0x3c000000, v154
	v_rsq_f32_e32 v115, v115
	s_waitcnt vmcnt(2)
	v_pk_mul_f32 v[120:121], v[142:143], v[140:141]
	v_mov_b32_e32 v124, v102
	v_mov_b32_e32 v125, v98
	v_mul_f32_e32 v122, v158, v115
	v_pk_mul_f32 v[116:117], v[144:145], v[140:141]
	v_pk_fma_f32 v[120:121], v[144:145], v[138:139], v[120:121]
	v_pk_mul_f32 v[124:125], v[124:125], v[122:123] op_sel_hi:[1,0]
	v_pk_mul_f32 v[122:123], v[126:127], v[122:123] op_sel_hi:[1,0]
	v_pk_fma_f32 v[116:117], v[142:143], v[138:139], v[116:117] neg_lo:[0,0,1] neg_hi:[0,0,1]
	v_pk_mul_f32 v[126:127], v[120:121], v[122:123]
	v_and_or_b32 v115, v183, s1, v161
	v_pk_fma_f32 v[126:127], v[116:117], v[124:125], v[126:127]
	v_pk_mul_f32 v[124:125], v[120:121], v[124:125]
	v_mad_u32_u24 v115, v115, s0, v162
	v_pk_fma_f32 v[122:123], v[116:117], v[122:123], v[124:125] neg_lo:[0,0,1] neg_hi:[0,0,1]
	v_cvt_pk_f16_f32 v98, v126, v127
	v_cvt_pk_f16_f32 v102, v122, v123
	v_add_u32_e32 v106, 0x1000, v115
	ds_write2_b32 v106, v98, v102 offset1:32
	s_waitcnt lgkmcnt(5)
	v_add_f32_e32 v98, v128, v129
	v_fmamk_f32 v98, v98, 0x3c000000, v154
	v_rsq_f32_e32 v98, v98
	v_pk_mul_f32 v[124:125], v[132:133], v[120:121]
	v_mov_b32_e32 v110, v107
	v_pk_mul_f32 v[122:123], v[134:135], v[120:121]
	v_mul_f32_e32 v102, v158, v98
	v_or_b32_sdwa v98, v161, v201 dst_sel:DWORD dst_unused:UNUSED_PAD src0_sel:DWORD src1_sel:WORD_0
	v_mad_u32_u24 v115, v98, s0, v162
	v_mov_b32_e32 v98, v103
	v_pk_fma_f32 v[124:125], v[134:135], v[116:117], v[124:125]
	v_pk_mul_f32 v[98:99], v[98:99], v[102:103] op_sel_hi:[1,0]
	v_pk_mul_f32 v[102:103], v[110:111], v[102:103] op_sel_hi:[1,0]
	v_pk_fma_f32 v[122:123], v[132:133], v[116:117], v[122:123] neg_lo:[0,0,1] neg_hi:[0,0,1]
	v_pk_mul_f32 v[106:107], v[124:125], v[102:103]
	s_movk_i32 s4, 0x7c
	v_pk_fma_f32 v[106:107], v[122:123], v[98:99], v[106:107]
	v_pk_mul_f32 v[98:99], v[124:125], v[98:99]
	v_cvt_pk_f16_f32 v106, v106, v107
	v_pk_fma_f32 v[98:99], v[122:123], v[102:103], v[98:99] neg_lo:[0,0,1] neg_hi:[0,0,1]
	v_pk_mul_f32 v[102:103], v[134:135], v[124:125]
	v_cvt_pk_f16_f32 v99, v98, v99
	v_add_u32_e32 v98, 0x1000, v115
	ds_write2_b32 v98, v106, v99 offset0:68 offset1:100
	s_waitcnt lgkmcnt(4)
	v_add_f32_e32 v99, v184, v185
	v_fmamk_f32 v99, v99, 0x3c000000, v154
	v_rsq_f32_e32 v99, v99
	v_pk_mul_f32 v[106:107], v[132:133], v[124:125]
	v_pk_fma_f32 v[102:103], v[132:133], v[122:123], v[102:103] neg_lo:[0,0,1] neg_hi:[0,0,1]
	v_pk_fma_f32 v[106:107], v[134:135], v[122:123], v[106:107]
	v_mul_f32_e32 v110, v158, v99
	v_mov_b32_e32 v122, v104
	v_mov_b32_e32 v123, v100
	v_mov_b32_e32 v124, v108
	v_mov_b32_e32 v125, v112
	v_pk_mul_f32 v[122:123], v[122:123], v[110:111] op_sel_hi:[1,0]
	v_pk_mul_f32 v[110:111], v[124:125], v[110:111] op_sel_hi:[1,0]
	v_mov_b32_e32 v112, v109
	v_pk_mul_f32 v[124:125], v[106:107], v[110:111]
	v_mov_b32_e32 v109, v94
	v_pk_fma_f32 v[124:125], v[102:103], v[122:123], v[124:125]
	v_pk_mul_f32 v[122:123], v[106:107], v[122:123]
	v_cvt_pk_f16_f32 v99, v124, v125
	v_pk_fma_f32 v[110:111], v[102:103], v[110:111], v[122:123] neg_lo:[0,0,1] neg_hi:[0,0,1]
	v_mov_b32_e32 v94, v91
	v_cvt_pk_f16_f32 v100, v110, v111
	ds_write2_b32 v98, v99, v100 offset0:136 offset1:168
	s_waitcnt lgkmcnt(3)
	v_add_f32_e32 v99, v186, v187
	v_fmamk_f32 v99, v99, 0x3c000000, v154
	v_rsq_f32_e32 v99, v99
	v_pk_mul_f32 v[110:111], v[134:135], v[106:107]
	v_pk_mul_f32 v[106:107], v[132:133], v[106:107]
	v_mov_b32_e32 v100, v105
	v_mul_f32_e32 v104, v158, v99
	v_pk_fma_f32 v[110:111], v[132:133], v[102:103], v[110:111] neg_lo:[0,0,1] neg_hi:[0,0,1]
	v_pk_fma_f32 v[102:103], v[134:135], v[102:103], v[106:107]
	v_pk_mul_f32 v[100:101], v[100:101], v[104:105] op_sel_hi:[1,0]
	v_pk_mul_f32 v[104:105], v[112:113], v[104:105] op_sel_hi:[1,0]
	v_mad_u32_u24 v155, v152, s0, v182
	v_pk_mul_f32 v[106:107], v[102:103], v[104:105]
	s_or_b32 s5, s2, 0x1000
	v_pk_fma_f32 v[106:107], v[110:111], v[100:101], v[106:107]
	v_pk_mul_f32 v[100:101], v[102:103], v[100:101]
	v_cvt_pk_f16_f32 v99, v106, v107
	v_pk_fma_f32 v[100:101], v[110:111], v[104:105], v[100:101] neg_lo:[0,0,1] neg_hi:[0,0,1]
	v_lshlrev_b32_e32 v103, 2, v181
	v_cvt_pk_f16_f32 v100, v100, v101
	ds_write2_b32 v98, v99, v100 offset0:204 offset1:236
	v_lshlrev_b32_e32 v99, 2, v178
	v_or_b32_e32 v102, v99, v1
	v_bitop3_b32 v99, v99, 1, v1 bitop3:0x36
	v_lshlrev_b32_e32 v105, 2, v180
	v_lshlrev_b32_e32 v107, 2, v179
	v_lshl_add_u32 v102, v102, 2, 0
	v_lshl_add_u32 v99, v99, 2, 0
	v_or_b32_e32 v104, v103, v1
	v_bitop3_b32 v103, v103, 1, v1 bitop3:0x36
	v_or_b32_e32 v106, v105, v1
	v_bitop3_b32 v105, v105, 1, v1 bitop3:0x36
	v_or_b32_e32 v108, v107, v1
	v_bitop3_b32 v107, v107, 1, v1 bitop3:0x36
	v_lshl_add_u32 v104, v104, 2, 0
	v_lshl_add_u32 v103, v103, 2, 0
	v_lshl_add_u32 v106, v106, 2, 0
	v_lshl_add_u32 v105, v105, 2, 0
	v_lshl_add_u32 v108, v108, 2, 0
	v_lshl_add_u32 v107, v107, 2, 0
	ds_read_b32 v102, v102
	ds_read_b32 v99, v99
	ds_read_b32 v110, v104
	ds_read_b32 v111, v103
	ds_read_b32 v112, v106
	ds_read_b32 v113, v105
	ds_read_b32 v115, v108
	ds_read_b32 v119, v107
	s_waitcnt lgkmcnt(6)
	v_add_f32_e32 v99, v102, v99
	v_fmamk_f32 v99, v99, 0x3c000000, v154
	v_rsq_f32_e32 v99, v99
	v_pk_mul_f32 v[102:103], v[138:139], v[120:121]
	v_mov_b32_e32 v106, v86
	v_mov_b32_e32 v107, v82
	v_mul_f32_e32 v104, v158, v99
	v_mov_b32_e32 v108, v90
	v_pk_mul_f32 v[100:101], v[140:141], v[120:121]
	v_pk_fma_f32 v[102:103], v[140:141], v[116:117], v[102:103]
	v_pk_mul_f32 v[106:107], v[106:107], v[104:105] op_sel_hi:[1,0]
	v_pk_mul_f32 v[104:105], v[108:109], v[104:105] op_sel_hi:[1,0]
	v_pk_fma_f32 v[100:101], v[138:139], v[116:117], v[100:101] neg_lo:[0,0,1] neg_hi:[0,0,1]
	v_pk_mul_f32 v[108:109], v[102:103], v[104:105]
	v_and_or_b32 v99, v178, s3, v161
	v_pk_fma_f32 v[108:109], v[100:101], v[106:107], v[108:109]
	v_pk_mul_f32 v[106:107], v[102:103], v[106:107]
	v_mad_u32_u24 v99, v99, s0, v162
	v_pk_fma_f32 v[104:105], v[100:101], v[104:105], v[106:107] neg_lo:[0,0,1] neg_hi:[0,0,1]
	v_cvt_pk_f16_f32 v82, v108, v109
	v_cvt_pk_f16_f32 v86, v104, v105
	v_add_u32_e32 v90, 0x1000, v99
	ds_write2_b32 v90, v82, v86 offset1:32
	s_waitcnt lgkmcnt(5)
	v_add_f32_e32 v82, v110, v111
	v_fmamk_f32 v82, v82, 0x3c000000, v154
	v_rsq_f32_e32 v82, v82
	v_pk_mul_f32 v[106:107], v[132:133], v[102:103]
	v_pk_mul_f32 v[104:105], v[134:135], v[102:103]
	v_pk_fma_f32 v[106:107], v[134:135], v[100:101], v[106:107]
	v_mul_f32_e32 v86, v158, v82
	v_or_b32_sdwa v82, v161, v202 dst_sel:DWORD dst_unused:UNUSED_PAD src0_sel:DWORD src1_sel:WORD_0
	v_mad_u32_u24 v99, v82, s0, v162
	v_mov_b32_e32 v82, v87
	v_pk_mul_f32 v[82:83], v[82:83], v[86:87] op_sel_hi:[1,0]
	v_pk_mul_f32 v[86:87], v[94:95], v[86:87] op_sel_hi:[1,0]
	v_pk_fma_f32 v[104:105], v[132:133], v[100:101], v[104:105] neg_lo:[0,0,1] neg_hi:[0,0,1]
	v_pk_mul_f32 v[90:91], v[106:107], v[86:87]
	s_waitcnt vmcnt(0)
	v_pk_mul_f32 v[150:151], v[144:145], v[148:149]
	v_pk_fma_f32 v[90:91], v[104:105], v[82:83], v[90:91]
	v_pk_mul_f32 v[82:83], v[106:107], v[82:83]
	v_cvt_pk_f16_f32 v90, v90, v91
	v_pk_fma_f32 v[82:83], v[104:105], v[86:87], v[82:83] neg_lo:[0,0,1] neg_hi:[0,0,1]
	v_pk_mul_f32 v[86:87], v[134:135], v[106:107]
	v_cvt_pk_f16_f32 v83, v82, v83
	v_add_u32_e32 v82, 0x1000, v99
	ds_write2_b32 v82, v90, v83 offset0:68 offset1:100
	s_waitcnt lgkmcnt(4)
	v_add_f32_e32 v83, v112, v113
	v_fmamk_f32 v83, v83, 0x3c000000, v154
	v_rsq_f32_e32 v83, v83
	v_pk_mul_f32 v[90:91], v[132:133], v[106:107]
	v_pk_fma_f32 v[86:87], v[132:133], v[104:105], v[86:87] neg_lo:[0,0,1] neg_hi:[0,0,1]
	v_pk_fma_f32 v[90:91], v[134:135], v[104:105], v[90:91]
	v_mul_f32_e32 v94, v158, v83
	v_mov_b32_e32 v104, v88
	v_mov_b32_e32 v105, v84
	v_mov_b32_e32 v106, v92
	v_mov_b32_e32 v107, v96
	v_pk_mul_f32 v[104:105], v[104:105], v[94:95] op_sel_hi:[1,0]
	v_pk_mul_f32 v[94:95], v[106:107], v[94:95] op_sel_hi:[1,0]
	v_mov_b32_e32 v96, v93
	v_pk_mul_f32 v[106:107], v[90:91], v[94:95]
	v_mov_b32_e32 v93, v78
	v_pk_fma_f32 v[106:107], v[86:87], v[104:105], v[106:107]
	v_pk_mul_f32 v[104:105], v[90:91], v[104:105]
	v_cvt_pk_f16_f32 v83, v106, v107
	v_pk_fma_f32 v[94:95], v[86:87], v[94:95], v[104:105] neg_lo:[0,0,1] neg_hi:[0,0,1]
	v_mov_b32_e32 v78, v75
	v_cvt_pk_f16_f32 v84, v94, v95
	ds_write2_b32 v82, v83, v84 offset0:136 offset1:168
	s_waitcnt lgkmcnt(3)
	v_add_f32_e32 v83, v115, v119
	v_fmamk_f32 v83, v83, 0x3c000000, v154
	v_rsq_f32_e32 v83, v83
	v_pk_mul_f32 v[94:95], v[134:135], v[90:91]
	v_pk_mul_f32 v[90:91], v[132:133], v[90:91]
	v_mov_b32_e32 v84, v89
	v_mul_f32_e32 v88, v158, v83
	v_pk_fma_f32 v[94:95], v[132:133], v[86:87], v[94:95] neg_lo:[0,0,1] neg_hi:[0,0,1]
	v_pk_fma_f32 v[86:87], v[134:135], v[86:87], v[90:91]
	v_pk_mul_f32 v[84:85], v[84:85], v[88:89] op_sel_hi:[1,0]
	v_pk_mul_f32 v[88:89], v[96:97], v[88:89] op_sel_hi:[1,0]
	s_nop 0
	v_pk_mul_f32 v[90:91], v[86:87], v[88:89]
	s_nop 0
	v_pk_fma_f32 v[90:91], v[94:95], v[84:85], v[90:91]
	v_pk_mul_f32 v[84:85], v[86:87], v[84:85]
	v_cvt_pk_f16_f32 v83, v90, v91
	v_pk_fma_f32 v[84:85], v[94:95], v[88:89], v[84:85] neg_lo:[0,0,1] neg_hi:[0,0,1]
	v_lshlrev_b32_e32 v87, 2, v177
	v_cvt_pk_f16_f32 v84, v84, v85
	ds_write2_b32 v82, v83, v84 offset0:204 offset1:236
	v_lshlrev_b32_e32 v83, 2, v174
	v_or_b32_e32 v86, v83, v1
	v_bitop3_b32 v83, v83, 1, v1 bitop3:0x36
	v_lshlrev_b32_e32 v89, 2, v176
	v_lshlrev_b32_e32 v91, 2, v175
	v_lshl_add_u32 v86, v86, 2, 0
	v_lshl_add_u32 v83, v83, 2, 0
	v_or_b32_e32 v88, v87, v1
	v_bitop3_b32 v87, v87, 1, v1 bitop3:0x36
	v_or_b32_e32 v90, v89, v1
	v_bitop3_b32 v89, v89, 1, v1 bitop3:0x36
	v_or_b32_e32 v92, v91, v1
	v_bitop3_b32 v91, v91, 1, v1 bitop3:0x36
	v_lshl_add_u32 v88, v88, 2, 0
	v_lshl_add_u32 v87, v87, 2, 0
	v_lshl_add_u32 v90, v90, 2, 0
	v_lshl_add_u32 v89, v89, 2, 0
	v_lshl_add_u32 v92, v92, 2, 0
	v_lshl_add_u32 v91, v91, 2, 0
	ds_read_b32 v86, v86
	ds_read_b32 v83, v83
	ds_read_b32 v94, v88
	ds_read_b32 v95, v87
	ds_read_b32 v96, v90
	ds_read_b32 v97, v89
	ds_read_b32 v99, v92
	ds_read_b32 v104, v91
	s_waitcnt lgkmcnt(6)
	v_add_f32_e32 v83, v86, v83
	v_fmamk_f32 v83, v83, 0x3c000000, v154
	v_rsq_f32_e32 v83, v83
	v_pk_mul_f32 v[86:87], v[138:139], v[102:103]
	v_mov_b32_e32 v90, v70
	v_mov_b32_e32 v91, v66
	v_mul_f32_e32 v88, v158, v83
	v_mov_b32_e32 v92, v74
	v_pk_mul_f32 v[84:85], v[140:141], v[102:103]
	v_pk_fma_f32 v[86:87], v[140:141], v[100:101], v[86:87]
	v_pk_mul_f32 v[90:91], v[90:91], v[88:89] op_sel_hi:[1,0]
	v_pk_mul_f32 v[88:89], v[92:93], v[88:89] op_sel_hi:[1,0]
	v_pk_fma_f32 v[84:85], v[138:139], v[100:101], v[84:85] neg_lo:[0,0,1] neg_hi:[0,0,1]
	v_pk_mul_f32 v[92:93], v[86:87], v[88:89]
	v_and_or_b32 v83, v174, s4, v161
	v_pk_fma_f32 v[92:93], v[84:85], v[90:91], v[92:93]
	v_pk_mul_f32 v[90:91], v[86:87], v[90:91]
	v_mad_u32_u24 v83, v83, s0, v162
	v_pk_fma_f32 v[88:89], v[84:85], v[88:89], v[90:91] neg_lo:[0,0,1] neg_hi:[0,0,1]
	v_cvt_pk_f16_f32 v66, v92, v93
	v_cvt_pk_f16_f32 v70, v88, v89
	v_add_u32_e32 v74, 0x1000, v83
	ds_write2_b32 v74, v66, v70 offset1:32
	s_waitcnt lgkmcnt(5)
	v_add_f32_e32 v66, v94, v95
	v_fmamk_f32 v66, v66, 0x3c000000, v154
	v_rsq_f32_e32 v66, v66
	v_pk_mul_f32 v[88:89], v[134:135], v[86:87]
	v_pk_mul_f32 v[86:87], v[132:133], v[86:87]
	v_pk_fma_f32 v[88:89], v[132:133], v[84:85], v[88:89] neg_lo:[0,0,1] neg_hi:[0,0,1]
	v_mul_f32_e32 v70, v158, v66
	v_or_b32_sdwa v66, v161, v130 dst_sel:DWORD dst_unused:UNUSED_PAD src0_sel:DWORD src1_sel:WORD_0
	v_mad_u32_u24 v83, v66, s0, v162
	v_mov_b32_e32 v66, v71
	v_pk_fma_f32 v[84:85], v[134:135], v[84:85], v[86:87]
	v_pk_mul_f32 v[66:67], v[66:67], v[70:71] op_sel_hi:[1,0]
	v_pk_mul_f32 v[70:71], v[78:79], v[70:71] op_sel_hi:[1,0]
	v_mov_b32_e32 v78, v72
	v_pk_mul_f32 v[74:75], v[84:85], v[70:71]
	v_mov_b32_e32 v79, v68
	v_pk_fma_f32 v[74:75], v[88:89], v[66:67], v[74:75]
	v_pk_mul_f32 v[66:67], v[84:85], v[66:67]
	v_cvt_pk_f16_f32 v74, v74, v75
	v_pk_fma_f32 v[66:67], v[88:89], v[70:71], v[66:67] neg_lo:[0,0,1] neg_hi:[0,0,1]
	v_pk_mul_f32 v[70:71], v[134:135], v[84:85]
	v_cvt_pk_f16_f32 v66, v66, v67
	v_add_u32_e32 v67, 0x1000, v83
	ds_write2_b32 v67, v74, v66 offset0:68 offset1:100
	s_waitcnt lgkmcnt(4)
	v_add_f32_e32 v66, v96, v97
	v_fmamk_f32 v66, v66, 0x3c000000, v154
	v_rsq_f32_e32 v66, v66
	v_pk_mul_f32 v[74:75], v[132:133], v[84:85]
	v_mov_b32_e32 v84, v76
	v_mov_b32_e32 v85, v80
	v_mul_f32_e32 v66, v158, v66
	v_pk_fma_f32 v[74:75], v[134:135], v[88:89], v[74:75]
	v_pk_mul_f32 v[84:85], v[84:85], v[66:67] op_sel_hi:[1,0]
	v_pk_fma_f32 v[70:71], v[132:133], v[88:89], v[70:71] neg_lo:[0,0,1] neg_hi:[0,0,1]
	v_pk_mul_f32 v[78:79], v[78:79], v[66:67] op_sel_hi:[1,0]
	v_pk_mul_f32 v[86:87], v[74:75], v[84:85]
	v_mov_b32_e32 v80, v77
	v_pk_fma_f32 v[86:87], v[70:71], v[78:79], v[86:87]
	v_pk_mul_f32 v[78:79], v[74:75], v[78:79]
	v_cvt_pk_f16_f32 v66, v86, v87
	v_pk_fma_f32 v[78:79], v[70:71], v[84:85], v[78:79] neg_lo:[0,0,1] neg_hi:[0,0,1]
	s_nop 0
	v_cvt_pk_f16_f32 v68, v78, v79
	ds_write2_b32 v67, v66, v68 offset0:136 offset1:168
	s_waitcnt lgkmcnt(3)
	v_add_f32_e32 v66, v99, v104
	v_fmamk_f32 v66, v66, 0x3c000000, v154
	v_rsq_f32_e32 v66, v66
	v_pk_mul_f32 v[78:79], v[134:135], v[74:75]
	v_pk_mul_f32 v[74:75], v[132:133], v[74:75]
	v_pk_fma_f32 v[78:79], v[132:133], v[70:71], v[78:79] neg_lo:[0,0,1] neg_hi:[0,0,1]
	v_mul_f32_e32 v66, v158, v66
	v_pk_fma_f32 v[70:71], v[134:135], v[70:71], v[74:75]
	v_mov_b32_e32 v68, v73
	v_pk_mul_f32 v[72:73], v[80:81], v[66:67] op_sel_hi:[1,0]
	v_pk_mul_f32 v[68:69], v[68:69], v[66:67] op_sel_hi:[1,0]
	v_pk_mul_f32 v[74:75], v[70:71], v[72:73]
	s_nop 0
	v_pk_fma_f32 v[74:75], v[78:79], v[68:69], v[74:75]
	v_pk_mul_f32 v[68:69], v[70:71], v[68:69]
	v_cvt_pk_f16_f32 v66, v74, v75
	v_pk_fma_f32 v[68:69], v[78:79], v[72:73], v[68:69] neg_lo:[0,0,1] neg_hi:[0,0,1]
	s_nop 0
	v_cvt_pk_f16_f32 v68, v68, v69
	ds_write2_b32 v67, v66, v68 offset0:204 offset1:236
	s_waitcnt lgkmcnt(0)
	s_barrier
	ds_read_b128 v[70:73], v155 offset:4096
	v_or_b32_e32 v66, s2, v152
	v_lshlrev_b32_e32 v130, 8, v66
	v_or_b32_e32 v66, 0x200, v0
	v_lshrrev_b32_e32 v66, 4, v66
	v_lshl_add_u64 v[78:79], v[136:137], 0, v[130:131]
	v_mad_u32_u24 v68, v66, s0, v182
	v_or_b32_e32 v69, s2, v66
	ds_read_b128 v[74:77], v68 offset:38912
	s_waitcnt lgkmcnt(1)
	global_store_dwordx4 v[78:79], v[70:73], off sc1
	ds_read_b128 v[78:81], v68 offset:4096
	v_lshlrev_b32_e32 v130, 8, v69
	v_or_b32_e32 v69, 64, v152
	v_mad_u32_u24 v70, v69, s0, v182
	ds_read_b128 v[84:87], v70 offset:4096
	v_or_b32_e32 v0, 0x600, v0
	v_or_b32_e32 v71, s2, v69
	v_lshrrev_b32_e32 v0, 4, v0
	v_lshl_add_u64 v[72:73], v[136:137], 0, v[130:131]
	v_lshlrev_b32_e32 v130, 8, v71
	v_mad_u32_u24 v71, v0, s0, v182
	s_waitcnt lgkmcnt(1)
	global_store_dwordx4 v[72:73], v[78:81], off sc1
	ds_read_b128 v[78:81], v71 offset:4096
	v_lshl_add_u64 v[72:73], v[136:137], 0, v[130:131]
	s_waitcnt lgkmcnt(1)
	global_store_dwordx4 v[72:73], v[84:87], off sc1
	v_or_b32_e32 v72, s2, v0
	v_lshlrev_b32_e32 v130, 8, v72
	v_or_b32_e32 v72, 0x80, v0
	v_lshl_add_u64 v[88:89], v[136:137], 0, v[130:131]
	v_mad_u32_u24 v72, v72, s0, v182
	ds_read_b128 v[84:87], v72 offset:4096
	s_waitcnt lgkmcnt(1)
	global_store_dwordx4 v[88:89], v[78:81], off sc1
	ds_read_b128 v[78:81], v155 offset:38912
	v_or_b32_e32 v73, s5, v152
	ds_read_b128 v[88:91], v155 offset:56320
	v_lshlrev_b32_e32 v130, 8, v73
	v_or_b32_e32 v73, s5, v66
	v_lshl_add_u64 v[92:93], v[136:137], 0, v[130:131]
	v_lshlrev_b32_e32 v130, 8, v73
	v_or_b32_e32 v73, s5, v69
	s_waitcnt lgkmcnt(1)
	global_store_dwordx4 v[92:93], v[78:81], off sc1
	s_nop 1
	v_lshl_add_u64 v[78:79], v[136:137], 0, v[130:131]
	v_lshlrev_b32_e32 v130, 8, v73
	v_or_b32_e32 v73, s5, v0
	global_store_dwordx4 v[78:79], v[74:77], off sc1
	v_lshlrev_b32_e32 v79, 2, v170
	v_or_b32_e32 v80, v79, v1
	v_lshl_add_u64 v[74:75], v[136:137], 0, v[130:131]
	v_lshlrev_b32_e32 v130, 8, v73
	s_waitcnt lgkmcnt(0)
	global_store_dwordx4 v[74:75], v[88:91], off sc1
	v_lshl_add_u64 v[74:75], v[136:137], 0, v[130:131]
	v_lshlrev_b32_e32 v73, 2, v173
	global_store_dwordx4 v[74:75], v[84:87], off sc1
	v_or_b32_e32 v74, v73, v1
	v_bitop3_b32 v73, v73, 1, v1 bitop3:0x36
	v_lshlrev_b32_e32 v75, 2, v172
	v_lshlrev_b32_e32 v77, 2, v171
	v_lshl_add_u32 v74, v74, 2, 0
	v_lshl_add_u32 v73, v73, 2, 0
	v_or_b32_e32 v76, v75, v1
	v_bitop3_b32 v75, v75, 1, v1 bitop3:0x36
	v_or_b32_e32 v78, v77, v1
	v_bitop3_b32 v77, v77, 1, v1 bitop3:0x36
	v_bitop3_b32 v79, v79, 1, v1 bitop3:0x36
	s_barrier
	v_lshl_add_u32 v76, v76, 2, 0
	v_lshl_add_u32 v75, v75, 2, 0
	v_lshl_add_u32 v78, v78, 2, 0
	v_lshl_add_u32 v77, v77, 2, 0
	v_lshl_add_u32 v80, v80, 2, 0
	v_lshl_add_u32 v79, v79, 2, 0
	ds_read_b32 v74, v74
	ds_read_b32 v73, v73
	ds_read_b32 v83, v76
	ds_read_b32 v86, v75
	ds_read_b32 v87, v78
	ds_read_b32 v88, v77
	ds_read_b32 v89, v80
	ds_read_b32 v90, v79
	s_waitcnt lgkmcnt(6)
	v_add_f32_e32 v73, v74, v73
	v_fmamk_f32 v73, v73, 0x3c000000, v154
	v_rsq_f32_e32 v73, v73
	v_pk_mul_f32 v[76:77], v[142:143], v[148:149]
	v_mov_b32_e32 v80, v54
	v_mov_b32_e32 v81, v50
	v_mul_f32_e32 v78, v158, v73
	v_mov_b32_e32 v84, v58
	v_mov_b32_e32 v85, v62
	v_pk_fma_f32 v[76:77], v[144:145], v[146:147], v[76:77]
	v_pk_mul_f32 v[80:81], v[80:81], v[78:79] op_sel_hi:[1,0]
	v_pk_mul_f32 v[78:79], v[84:85], v[78:79] op_sel_hi:[1,0]
	v_pk_fma_f32 v[74:75], v[142:143], v[146:147], v[150:151] neg_lo:[0,0,1] neg_hi:[0,0,1]
	v_pk_mul_f32 v[84:85], v[76:77], v[78:79]
	v_mov_b32_e32 v62, v59
	v_pk_fma_f32 v[84:85], v[74:75], v[80:81], v[84:85]
	v_pk_mul_f32 v[80:81], v[76:77], v[80:81]
	v_cvt_pk_f16_f32 v50, v84, v85
	v_pk_fma_f32 v[78:79], v[74:75], v[78:79], v[80:81] neg_lo:[0,0,1] neg_hi:[0,0,1]
	v_pk_mul_f32 v[80:81], v[132:133], v[76:77]
	v_cvt_pk_f16_f32 v54, v78, v79
	ds_write2_b32 v118, v50, v54 offset1:32
	s_waitcnt lgkmcnt(5)
	v_add_f32_e32 v50, v83, v86
	v_fmamk_f32 v50, v50, 0x3c000000, v154
	v_rsq_f32_e32 v50, v50
	v_pk_mul_f32 v[78:79], v[134:135], v[76:77]
	v_pk_fma_f32 v[80:81], v[134:135], v[74:75], v[80:81]
	v_pk_fma_f32 v[78:79], v[132:133], v[74:75], v[78:79] neg_lo:[0,0,1] neg_hi:[0,0,1]
	v_mul_f32_e32 v54, v158, v50
	v_mov_b32_e32 v50, v55
	v_pk_mul_f32 v[50:51], v[50:51], v[54:55] op_sel_hi:[1,0]
	v_pk_mul_f32 v[54:55], v[62:63], v[54:55] op_sel_hi:[1,0]
	v_mov_b32_e32 v62, v56
	v_pk_mul_f32 v[58:59], v[80:81], v[54:55]
	v_mov_b32_e32 v63, v52
	v_pk_fma_f32 v[58:59], v[78:79], v[50:51], v[58:59]
	v_pk_mul_f32 v[50:51], v[80:81], v[50:51]
	v_cvt_pk_f16_f32 v58, v58, v59
	v_pk_fma_f32 v[50:51], v[78:79], v[54:55], v[50:51] neg_lo:[0,0,1] neg_hi:[0,0,1]
	s_waitcnt lgkmcnt(3)
	v_add_f32_e32 v54, v87, v88
	v_cvt_pk_f16_f32 v50, v50, v51
	v_fmamk_f32 v54, v54, 0x3c000000, v154
	ds_write2_b32 v114, v58, v50 offset0:68 offset1:100
	v_rsq_f32_e32 v58, v54
	v_pk_mul_f32 v[50:51], v[134:135], v[80:81]
	v_pk_mul_f32 v[54:55], v[132:133], v[80:81]
	v_pk_fma_f32 v[50:51], v[132:133], v[78:79], v[50:51] neg_lo:[0,0,1] neg_hi:[0,0,1]
	v_pk_fma_f32 v[54:55], v[134:135], v[78:79], v[54:55]
	v_mul_f32_e32 v58, v158, v58
	v_mov_b32_e32 v78, v60
	v_mov_b32_e32 v79, v64
	v_pk_mul_f32 v[62:63], v[62:63], v[58:59] op_sel_hi:[1,0]
	v_pk_mul_f32 v[58:59], v[78:79], v[58:59] op_sel_hi:[1,0]
	v_mov_b32_e32 v64, v61
	v_pk_mul_f32 v[78:79], v[54:55], v[58:59]
	s_nop 0
	v_pk_fma_f32 v[78:79], v[50:51], v[62:63], v[78:79]
	v_pk_mul_f32 v[62:63], v[54:55], v[62:63]
	v_cvt_pk_f16_f32 v52, v78, v79
	v_pk_fma_f32 v[58:59], v[50:51], v[58:59], v[62:63] neg_lo:[0,0,1] neg_hi:[0,0,1]
	s_nop 0
	v_cvt_pk_f16_f32 v56, v58, v59
	ds_write2_b32 v114, v52, v56 offset0:136 offset1:168
	s_waitcnt lgkmcnt(3)
	v_add_f32_e32 v52, v89, v90
	v_fmamk_f32 v52, v52, 0x3c000000, v154
	v_rsq_f32_e32 v52, v52
	v_pk_mul_f32 v[58:59], v[134:135], v[54:55]
	v_pk_mul_f32 v[54:55], v[132:133], v[54:55]
	v_pk_fma_f32 v[58:59], v[132:133], v[50:51], v[58:59] neg_lo:[0,0,1] neg_hi:[0,0,1]
	v_pk_fma_f32 v[50:51], v[134:135], v[50:51], v[54:55]
	v_mul_f32_e32 v54, v158, v52
	v_mov_b32_e32 v52, v57
	v_pk_mul_f32 v[52:53], v[52:53], v[54:55] op_sel_hi:[1,0]
	v_pk_mul_f32 v[54:55], v[64:65], v[54:55] op_sel_hi:[1,0]
	s_nop 0
	v_pk_mul_f32 v[56:57], v[50:51], v[54:55]
	v_pk_mul_f32 v[50:51], v[50:51], v[52:53]
	v_pk_fma_f32 v[56:57], v[58:59], v[52:53], v[56:57]
	v_pk_fma_f32 v[50:51], v[58:59], v[54:55], v[50:51] neg_lo:[0,0,1] neg_hi:[0,0,1]
	v_cvt_pk_f16_f32 v56, v56, v57
	v_cvt_pk_f16_f32 v50, v50, v51
	v_lshlrev_b32_e32 v52, 2, v166
	ds_write2_b32 v114, v56, v50 offset0:204 offset1:236
	v_or_b32_e32 v53, v52, v1
	v_bitop3_b32 v52, v52, 1, v1 bitop3:0x36
	v_lshlrev_b32_e32 v54, 2, v169
	v_lshlrev_b32_e32 v56, 2, v168
	v_lshlrev_b32_e32 v58, 2, v167
	v_lshl_add_u32 v53, v53, 2, 0
	v_lshl_add_u32 v52, v52, 2, 0
	v_or_b32_e32 v55, v54, v1
	v_bitop3_b32 v54, v54, 1, v1 bitop3:0x36
	v_or_b32_e32 v57, v56, v1
	v_bitop3_b32 v56, v56, 1, v1 bitop3:0x36
	v_or_b32_e32 v59, v58, v1
	v_bitop3_b32 v58, v58, 1, v1 bitop3:0x36
	v_lshl_add_u32 v55, v55, 2, 0
	v_lshl_add_u32 v54, v54, 2, 0
	v_lshl_add_u32 v57, v57, 2, 0
	v_lshl_add_u32 v56, v56, 2, 0
	v_lshl_add_u32 v59, v59, 2, 0
	v_lshl_add_u32 v58, v58, 2, 0
	ds_read_b32 v53, v53
	ds_read_b32 v52, v52
	ds_read_b32 v60, v55
	ds_read_b32 v61, v54
	ds_read_b32 v62, v57
	ds_read_b32 v63, v56
	ds_read_b32 v64, v59
	ds_read_b32 v65, v58
	s_waitcnt lgkmcnt(6)
	v_add_f32_e32 v52, v53, v52
	v_fmamk_f32 v52, v52, 0x3c000000, v154
	v_rsq_f32_e32 v54, v52
	v_pk_mul_f32 v[52:53], v[138:139], v[76:77]
	v_and_or_b32 v55, v166, s1, v161
	v_mov_b32_e32 v56, v38
	v_mul_f32_e32 v54, v158, v54
	v_mov_b32_e32 v57, v34
	v_mov_b32_e32 v58, v42
	v_mov_b32_e32 v59, v46
	v_pk_mul_f32 v[50:51], v[140:141], v[76:77]
	v_pk_fma_f32 v[52:53], v[140:141], v[74:75], v[52:53]
	v_mad_u32_u24 v73, v55, s0, v162
	v_pk_mul_f32 v[56:57], v[56:57], v[54:55] op_sel_hi:[1,0]
	v_pk_mul_f32 v[54:55], v[58:59], v[54:55] op_sel_hi:[1,0]
	v_pk_fma_f32 v[50:51], v[138:139], v[74:75], v[50:51] neg_lo:[0,0,1] neg_hi:[0,0,1]
	v_pk_mul_f32 v[58:59], v[52:53], v[54:55]
	v_add_u32_e32 v42, 0x1000, v73
	v_pk_fma_f32 v[58:59], v[50:51], v[56:57], v[58:59]
	v_pk_mul_f32 v[56:57], v[52:53], v[56:57]
	v_cvt_pk_f16_f32 v34, v58, v59
	v_pk_fma_f32 v[54:55], v[50:51], v[54:55], v[56:57] neg_lo:[0,0,1] neg_hi:[0,0,1]
	v_pk_mul_f32 v[56:57], v[132:133], v[52:53]
	v_cvt_pk_f16_f32 v38, v54, v55
	ds_write2_b32 v42, v34, v38 offset1:32
	s_waitcnt lgkmcnt(5)
	v_add_f32_e32 v34, v60, v61
	v_fmamk_f32 v34, v34, 0x3c000000, v154
	v_rsq_f32_e32 v34, v34
	v_mov_b32_e32 v46, v43
	v_pk_mul_f32 v[54:55], v[134:135], v[52:53]
	v_pk_fma_f32 v[56:57], v[134:135], v[50:51], v[56:57]
	v_mul_f32_e32 v38, v158, v34
	v_mov_b32_e32 v34, v39
	v_pk_mul_f32 v[34:35], v[34:35], v[38:39] op_sel_hi:[1,0]
	v_pk_mul_f32 v[38:39], v[46:47], v[38:39] op_sel_hi:[1,0]
	v_pk_fma_f32 v[54:55], v[132:133], v[50:51], v[54:55] neg_lo:[0,0,1] neg_hi:[0,0,1]
	v_pk_mul_f32 v[42:43], v[56:57], v[38:39]
	v_mov_b32_e32 v46, v40
	v_pk_fma_f32 v[42:43], v[54:55], v[34:35], v[42:43]
	v_pk_mul_f32 v[34:35], v[56:57], v[34:35]
	v_cvt_pk_f16_f32 v42, v42, v43
	v_pk_fma_f32 v[34:35], v[54:55], v[38:39], v[34:35] neg_lo:[0,0,1] neg_hi:[0,0,1]
	s_waitcnt lgkmcnt(3)
	v_add_f32_e32 v38, v62, v63
	v_cvt_pk_f16_f32 v34, v34, v35
	v_fmamk_f32 v38, v38, 0x3c000000, v154
	ds_write2_b32 v98, v42, v34 offset0:68 offset1:100
	v_rsq_f32_e32 v42, v38
	v_pk_mul_f32 v[34:35], v[134:135], v[56:57]
	v_pk_mul_f32 v[38:39], v[132:133], v[56:57]
	v_pk_fma_f32 v[34:35], v[132:133], v[54:55], v[34:35] neg_lo:[0,0,1] neg_hi:[0,0,1]
	v_pk_fma_f32 v[38:39], v[134:135], v[54:55], v[38:39]
	v_mul_f32_e32 v42, v158, v42
	v_mov_b32_e32 v47, v36
	v_mov_b32_e32 v54, v44
	v_mov_b32_e32 v55, v48
	v_pk_mul_f32 v[46:47], v[46:47], v[42:43] op_sel_hi:[1,0]
	v_pk_mul_f32 v[42:43], v[54:55], v[42:43] op_sel_hi:[1,0]
	v_mov_b32_e32 v48, v45
	v_pk_mul_f32 v[54:55], v[38:39], v[42:43]
	s_nop 0
	v_pk_fma_f32 v[54:55], v[34:35], v[46:47], v[54:55]
	v_pk_mul_f32 v[46:47], v[38:39], v[46:47]
	v_cvt_pk_f16_f32 v36, v54, v55
	v_pk_fma_f32 v[42:43], v[34:35], v[42:43], v[46:47] neg_lo:[0,0,1] neg_hi:[0,0,1]
	s_nop 0
	v_cvt_pk_f16_f32 v40, v42, v43
	ds_write2_b32 v98, v36, v40 offset0:136 offset1:168
	s_waitcnt lgkmcnt(3)
	v_add_f32_e32 v36, v64, v65
	v_fmamk_f32 v36, v36, 0x3c000000, v154
	v_rsq_f32_e32 v36, v36
	v_pk_mul_f32 v[42:43], v[134:135], v[38:39]
	v_pk_mul_f32 v[38:39], v[132:133], v[38:39]
	v_pk_fma_f32 v[42:43], v[132:133], v[34:35], v[42:43] neg_lo:[0,0,1] neg_hi:[0,0,1]
	v_pk_fma_f32 v[34:35], v[134:135], v[34:35], v[38:39]
	v_mul_f32_e32 v38, v158, v36
	v_mov_b32_e32 v36, v41
	v_pk_mul_f32 v[36:37], v[36:37], v[38:39] op_sel_hi:[1,0]
	v_pk_mul_f32 v[38:39], v[48:49], v[38:39] op_sel_hi:[1,0]
	s_nop 0
	v_pk_mul_f32 v[40:41], v[34:35], v[38:39]
	v_pk_mul_f32 v[34:35], v[34:35], v[36:37]
	v_pk_fma_f32 v[40:41], v[42:43], v[36:37], v[40:41]
	v_pk_fma_f32 v[34:35], v[42:43], v[38:39], v[34:35] neg_lo:[0,0,1] neg_hi:[0,0,1]
	v_cvt_pk_f16_f32 v40, v40, v41
	v_cvt_pk_f16_f32 v34, v34, v35
	v_lshlrev_b32_e32 v36, 2, v160
	ds_write2_b32 v98, v40, v34 offset0:204 offset1:236
	v_or_b32_e32 v37, v36, v1
	v_bitop3_b32 v36, v36, 1, v1 bitop3:0x36
	v_lshlrev_b32_e32 v38, 2, v165
	v_lshlrev_b32_e32 v40, 2, v164
	v_lshlrev_b32_e32 v42, 2, v163
	v_lshl_add_u32 v37, v37, 2, 0
	v_lshl_add_u32 v36, v36, 2, 0
	v_or_b32_e32 v39, v38, v1
	v_bitop3_b32 v38, v38, 1, v1 bitop3:0x36
	v_or_b32_e32 v41, v40, v1
	v_bitop3_b32 v40, v40, 1, v1 bitop3:0x36
	v_or_b32_e32 v43, v42, v1
	v_bitop3_b32 v42, v42, 1, v1 bitop3:0x36
	v_lshl_add_u32 v39, v39, 2, 0
	v_lshl_add_u32 v38, v38, 2, 0
	v_lshl_add_u32 v41, v41, 2, 0
	v_lshl_add_u32 v40, v40, 2, 0
	v_lshl_add_u32 v43, v43, 2, 0
	v_lshl_add_u32 v42, v42, 2, 0
	ds_read_b32 v37, v37
	ds_read_b32 v36, v36
	ds_read_b32 v44, v39
	ds_read_b32 v45, v38
	ds_read_b32 v46, v41
	ds_read_b32 v47, v40
	ds_read_b32 v48, v43
	ds_read_b32 v49, v42
	s_waitcnt lgkmcnt(6)
	v_add_f32_e32 v36, v37, v36
	v_fmamk_f32 v36, v36, 0x3c000000, v154
	v_rsq_f32_e32 v38, v36
	v_pk_mul_f32 v[34:35], v[140:141], v[52:53]
	v_pk_mul_f32 v[36:37], v[138:139], v[52:53]
	v_and_or_b32 v39, v160, s3, v161
	v_mul_f32_e32 v38, v158, v38
	v_mov_b32_e32 v40, v22
	v_mov_b32_e32 v41, v18
	v_mov_b32_e32 v42, v26
	v_mov_b32_e32 v43, v30
	v_pk_fma_f32 v[34:35], v[138:139], v[50:51], v[34:35] neg_lo:[0,0,1] neg_hi:[0,0,1]
	v_pk_fma_f32 v[36:37], v[140:141], v[50:51], v[36:37]
	v_mad_u32_u24 v50, v39, s0, v162
	v_pk_mul_f32 v[40:41], v[40:41], v[38:39] op_sel_hi:[1,0]
	v_pk_mul_f32 v[38:39], v[42:43], v[38:39] op_sel_hi:[1,0]
	v_add_u32_e32 v26, 0x1000, v50
	v_pk_mul_f32 v[42:43], v[36:37], v[38:39]
	v_mov_b32_e32 v30, v27
	v_pk_fma_f32 v[42:43], v[34:35], v[40:41], v[42:43]
	v_pk_mul_f32 v[40:41], v[36:37], v[40:41]
	v_cvt_pk_f16_f32 v18, v42, v43
	v_pk_fma_f32 v[38:39], v[34:35], v[38:39], v[40:41] neg_lo:[0,0,1] neg_hi:[0,0,1]
	v_pk_mul_f32 v[40:41], v[132:133], v[36:37]
	v_cvt_pk_f16_f32 v22, v38, v39
	ds_write2_b32 v26, v18, v22 offset1:32
	s_waitcnt lgkmcnt(5)
	v_add_f32_e32 v18, v44, v45
	v_fmamk_f32 v18, v18, 0x3c000000, v154
	v_rsq_f32_e32 v18, v18
	v_pk_mul_f32 v[38:39], v[134:135], v[36:37]
	v_pk_fma_f32 v[40:41], v[134:135], v[34:35], v[40:41]
	v_pk_fma_f32 v[38:39], v[132:133], v[34:35], v[38:39] neg_lo:[0,0,1] neg_hi:[0,0,1]
	v_mul_f32_e32 v22, v158, v18
	v_mov_b32_e32 v18, v23
	v_pk_mul_f32 v[18:19], v[18:19], v[22:23] op_sel_hi:[1,0]
	v_pk_mul_f32 v[22:23], v[30:31], v[22:23] op_sel_hi:[1,0]
	v_mov_b32_e32 v30, v24
	v_pk_mul_f32 v[26:27], v[40:41], v[22:23]
	v_mov_b32_e32 v31, v20
	v_pk_fma_f32 v[26:27], v[38:39], v[18:19], v[26:27]
	v_pk_mul_f32 v[18:19], v[40:41], v[18:19]
	v_cvt_pk_f16_f32 v26, v26, v27
	v_pk_fma_f32 v[18:19], v[38:39], v[22:23], v[18:19] neg_lo:[0,0,1] neg_hi:[0,0,1]
	s_waitcnt lgkmcnt(3)
	v_add_f32_e32 v22, v46, v47
	v_cvt_pk_f16_f32 v18, v18, v19
	v_fmamk_f32 v22, v22, 0x3c000000, v154
	ds_write2_b32 v82, v26, v18 offset0:68 offset1:100
	v_rsq_f32_e32 v26, v22
	v_pk_mul_f32 v[18:19], v[134:135], v[40:41]
	v_pk_mul_f32 v[22:23], v[132:133], v[40:41]
	v_pk_fma_f32 v[18:19], v[132:133], v[38:39], v[18:19] neg_lo:[0,0,1] neg_hi:[0,0,1]
	v_pk_fma_f32 v[22:23], v[134:135], v[38:39], v[22:23]
	v_mul_f32_e32 v26, v158, v26
	v_mov_b32_e32 v38, v28
	v_mov_b32_e32 v39, v32
	v_pk_mul_f32 v[30:31], v[30:31], v[26:27] op_sel_hi:[1,0]
	v_pk_mul_f32 v[26:27], v[38:39], v[26:27] op_sel_hi:[1,0]
	v_mov_b32_e32 v32, v29
	v_pk_mul_f32 v[38:39], v[22:23], v[26:27]
	s_nop 0
	v_pk_fma_f32 v[38:39], v[18:19], v[30:31], v[38:39]
	v_pk_mul_f32 v[30:31], v[22:23], v[30:31]
	v_cvt_pk_f16_f32 v20, v38, v39
	v_pk_fma_f32 v[26:27], v[18:19], v[26:27], v[30:31] neg_lo:[0,0,1] neg_hi:[0,0,1]
	s_nop 0
	v_cvt_pk_f16_f32 v24, v26, v27
	ds_write2_b32 v82, v20, v24 offset0:136 offset1:168
	s_waitcnt lgkmcnt(3)
	v_add_f32_e32 v20, v48, v49
	v_fmamk_f32 v20, v20, 0x3c000000, v154
	v_rsq_f32_e32 v20, v20
	v_pk_mul_f32 v[26:27], v[134:135], v[22:23]
	v_pk_mul_f32 v[22:23], v[132:133], v[22:23]
	v_pk_fma_f32 v[26:27], v[132:133], v[18:19], v[26:27] neg_lo:[0,0,1] neg_hi:[0,0,1]
	v_pk_fma_f32 v[18:19], v[134:135], v[18:19], v[22:23]
	v_mul_f32_e32 v22, v158, v20
	v_mov_b32_e32 v20, v25
	v_pk_mul_f32 v[20:21], v[20:21], v[22:23] op_sel_hi:[1,0]
	v_pk_mul_f32 v[22:23], v[32:33], v[22:23] op_sel_hi:[1,0]
	s_nop 0
	v_pk_mul_f32 v[24:25], v[18:19], v[22:23]
	v_pk_mul_f32 v[18:19], v[18:19], v[20:21]
	v_pk_fma_f32 v[24:25], v[26:27], v[20:21], v[24:25]
	v_pk_fma_f32 v[18:19], v[26:27], v[22:23], v[18:19] neg_lo:[0,0,1] neg_hi:[0,0,1]
	v_cvt_pk_f16_f32 v24, v24, v25
	v_cvt_pk_f16_f32 v18, v18, v19
	ds_write2_b32 v82, v24, v18 offset0:204 offset1:236
	v_lshlrev_b32_e32 v20, 2, v153
	v_lshlrev_b32_e32 v22, 2, v159
	v_lshlrev_b32_e32 v24, 2, v157
	v_lshlrev_b32_e32 v26, 2, v156
	v_or_b32_e32 v21, v20, v1
	v_bitop3_b32 v20, v20, 1, v1 bitop3:0x36
	v_or_b32_e32 v23, v22, v1
	v_bitop3_b32 v22, v22, 1, v1 bitop3:0x36
	v_or_b32_e32 v25, v24, v1
	v_bitop3_b32 v24, v24, 1, v1 bitop3:0x36
	v_or_b32_e32 v27, v26, v1
	v_bitop3_b32 v1, v26, 1, v1 bitop3:0x36
	v_lshl_add_u32 v21, v21, 2, 0
	v_lshl_add_u32 v20, v20, 2, 0
	v_lshl_add_u32 v1, v1, 2, 0
	v_lshl_add_u32 v23, v23, 2, 0
	v_lshl_add_u32 v22, v22, 2, 0
	v_lshl_add_u32 v25, v25, 2, 0
	v_lshl_add_u32 v24, v24, 2, 0
	v_lshl_add_u32 v27, v27, 2, 0
	ds_read_b32 v21, v21
	ds_read_b32 v20, v20
	ds_read_b32 v28, v23
	ds_read_b32 v29, v22
	ds_read_b32 v30, v25
	ds_read_b32 v31, v24
	ds_read_b32 v32, v27
	ds_read_b32 v1, v1
	s_waitcnt lgkmcnt(6)
	v_add_f32_e32 v20, v21, v20
	v_fmamk_f32 v20, v20, 0x3c000000, v154
	v_rsq_f32_e32 v22, v20
	v_pk_mul_f32 v[20:21], v[138:139], v[36:37]
	v_and_or_b32 v23, v153, s4, v161
	v_mov_b32_e32 v24, v6
	v_mul_f32_e32 v22, v158, v22
	v_mov_b32_e32 v25, v2
	v_mov_b32_e32 v26, v10
	v_mov_b32_e32 v27, v14
	v_pk_mul_f32 v[18:19], v[140:141], v[36:37]
	v_pk_fma_f32 v[20:21], v[140:141], v[34:35], v[20:21]
	v_mad_u32_u24 v33, v23, s0, v162
	v_pk_mul_f32 v[24:25], v[24:25], v[22:23] op_sel_hi:[1,0]
	v_pk_mul_f32 v[22:23], v[26:27], v[22:23] op_sel_hi:[1,0]
	v_pk_fma_f32 v[18:19], v[138:139], v[34:35], v[18:19] neg_lo:[0,0,1] neg_hi:[0,0,1]
	v_pk_mul_f32 v[26:27], v[20:21], v[22:23]
	v_add_u32_e32 v10, 0x1000, v33
	v_pk_fma_f32 v[26:27], v[18:19], v[24:25], v[26:27]
	v_pk_mul_f32 v[24:25], v[20:21], v[24:25]
	v_cvt_pk_f16_f32 v2, v26, v27
	v_pk_fma_f32 v[22:23], v[18:19], v[22:23], v[24:25] neg_lo:[0,0,1] neg_hi:[0,0,1]
	v_mov_b32_e32 v14, v11
	v_cvt_pk_f16_f32 v6, v22, v23
	ds_write2_b32 v10, v2, v6 offset1:32
	s_waitcnt lgkmcnt(5)
	v_add_f32_e32 v2, v28, v29
	v_fmamk_f32 v2, v2, 0x3c000000, v154
	v_rsq_f32_e32 v2, v2
	v_pk_mul_f32 v[22:23], v[134:135], v[20:21]
	v_pk_mul_f32 v[20:21], v[132:133], v[20:21]
	v_pk_fma_f32 v[22:23], v[132:133], v[18:19], v[22:23] neg_lo:[0,0,1] neg_hi:[0,0,1]
	v_mul_f32_e32 v6, v158, v2
	v_mov_b32_e32 v2, v7
	v_pk_fma_f32 v[18:19], v[134:135], v[18:19], v[20:21]
	v_pk_mul_f32 v[2:3], v[2:3], v[6:7] op_sel_hi:[1,0]
	v_pk_mul_f32 v[6:7], v[14:15], v[6:7] op_sel_hi:[1,0]
	v_mov_b32_e32 v14, v8
	v_pk_mul_f32 v[10:11], v[18:19], v[6:7]
	v_mov_b32_e32 v15, v4
	v_pk_fma_f32 v[10:11], v[22:23], v[2:3], v[10:11]
	v_pk_mul_f32 v[2:3], v[18:19], v[2:3]
	v_cvt_pk_f16_f32 v10, v10, v11
	v_pk_fma_f32 v[2:3], v[22:23], v[6:7], v[2:3] neg_lo:[0,0,1] neg_hi:[0,0,1]
	s_waitcnt lgkmcnt(3)
	v_add_f32_e32 v6, v30, v31
	v_cvt_pk_f16_f32 v2, v2, v3
	v_fmamk_f32 v6, v6, 0x3c000000, v154
	ds_write2_b32 v67, v10, v2 offset0:68 offset1:100
	v_rsq_f32_e32 v10, v6
	v_pk_mul_f32 v[2:3], v[134:135], v[18:19]
	v_pk_mul_f32 v[6:7], v[132:133], v[18:19]
	v_mov_b32_e32 v18, v12
	v_mul_f32_e32 v10, v158, v10
	v_mov_b32_e32 v19, v16
	s_waitcnt lgkmcnt(2)
	v_add_f32_e32 v1, v32, v1
	v_pk_fma_f32 v[6:7], v[134:135], v[22:23], v[6:7]
	v_pk_mul_f32 v[14:15], v[14:15], v[10:11] op_sel_hi:[1,0]
	v_pk_mul_f32 v[10:11], v[18:19], v[10:11] op_sel_hi:[1,0]
	v_fmac_f32_e32 v154, 0x3c000000, v1
	v_pk_fma_f32 v[2:3], v[132:133], v[22:23], v[2:3] neg_lo:[0,0,1] neg_hi:[0,0,1]
	v_pk_mul_f32 v[18:19], v[6:7], v[10:11]
	v_rsq_f32_e32 v1, v154
	v_pk_fma_f32 v[18:19], v[2:3], v[14:15], v[18:19]
	v_pk_mul_f32 v[14:15], v[6:7], v[14:15]
	v_cvt_pk_f16_f32 v4, v18, v19
	v_pk_fma_f32 v[10:11], v[2:3], v[10:11], v[14:15] neg_lo:[0,0,1] neg_hi:[0,0,1]
	v_mov_b32_e32 v16, v13
	v_cvt_pk_f16_f32 v8, v10, v11
	v_pk_mul_f32 v[10:11], v[134:135], v[6:7]
	v_pk_mul_f32 v[6:7], v[132:133], v[6:7]
	ds_write2_b32 v67, v4, v8 offset0:136 offset1:168
	v_pk_fma_f32 v[10:11], v[132:133], v[2:3], v[10:11] neg_lo:[0,0,1] neg_hi:[0,0,1]
	v_pk_fma_f32 v[2:3], v[134:135], v[2:3], v[6:7]
	v_mul_f32_e32 v6, v158, v1
	v_mov_b32_e32 v4, v9
	v_pk_mul_f32 v[4:5], v[4:5], v[6:7] op_sel_hi:[1,0]
	v_pk_mul_f32 v[6:7], v[16:17], v[6:7] op_sel_hi:[1,0]
	s_or_b32 s0, s2, 0x80
	v_pk_mul_f32 v[8:9], v[2:3], v[6:7]
	v_pk_mul_f32 v[2:3], v[2:3], v[4:5]
	v_pk_fma_f32 v[8:9], v[10:11], v[4:5], v[8:9]
	v_pk_fma_f32 v[2:3], v[10:11], v[6:7], v[2:3] neg_lo:[0,0,1] neg_hi:[0,0,1]
	v_cvt_pk_f16_f32 v1, v8, v9
	v_cvt_pk_f16_f32 v2, v2, v3
	ds_write2_b32 v67, v1, v2 offset0:204 offset1:236
	s_waitcnt lgkmcnt(0)
	s_barrier
	ds_read_b128 v[2:5], v155 offset:4096
	v_or_b32_e32 v1, s0, v152
	v_lshlrev_b32_e32 v130, 8, v1
	v_lshl_add_u64 v[10:11], v[136:137], 0, v[130:131]
	ds_read_b128 v[6:9], v68 offset:38912
	s_waitcnt lgkmcnt(1)
	global_store_dwordx4 v[10:11], v[2:5], off sc1
	ds_read_b128 v[2:5], v68 offset:4096
	ds_read_b128 v[10:13], v70 offset:4096
	v_or_b32_e32 v1, s0, v66
	v_lshlrev_b32_e32 v130, 8, v1
	v_or_b32_e32 v1, s0, v69
	v_lshl_add_u64 v[14:15], v[136:137], 0, v[130:131]
	v_lshlrev_b32_e32 v130, 8, v1
	s_waitcnt lgkmcnt(1)
	global_store_dwordx4 v[14:15], v[2:5], off sc1
	v_or_b32_e32 v1, s0, v0
	s_or_b32 s0, s2, 0x1080
	v_lshl_add_u64 v[2:3], v[136:137], 0, v[130:131]
	s_waitcnt lgkmcnt(0)
	global_store_dwordx4 v[2:3], v[10:13], off sc1
	ds_read_b128 v[2:5], v71 offset:4096
	ds_read_b128 v[10:13], v72 offset:4096
	v_lshlrev_b32_e32 v130, 8, v1
	v_lshl_add_u64 v[14:15], v[136:137], 0, v[130:131]
	v_or_b32_e32 v1, s0, v152
	s_waitcnt lgkmcnt(1)
	global_store_dwordx4 v[14:15], v[2:5], off sc1
	ds_read_b128 v[2:5], v155 offset:38912
	ds_read_b128 v[14:17], v155 offset:56320
	v_lshlrev_b32_e32 v130, 8, v1
	v_or_b32_e32 v1, s0, v66
	v_lshl_add_u64 v[18:19], v[136:137], 0, v[130:131]
	v_lshlrev_b32_e32 v130, 8, v1
	v_or_b32_e32 v1, s0, v69
	s_waitcnt lgkmcnt(1)
	global_store_dwordx4 v[18:19], v[2:5], off sc1
	v_or_b32_e32 v0, s0, v0
	s_nop 0
	v_lshl_add_u64 v[2:3], v[136:137], 0, v[130:131]
	v_lshlrev_b32_e32 v130, 8, v1
	global_store_dwordx4 v[2:3], v[6:9], off sc1
	v_lshl_add_u64 v[2:3], v[136:137], 0, v[130:131]
	v_lshlrev_b32_e32 v130, 8, v0
	v_lshl_add_u64 v[0:1], v[136:137], 0, v[130:131]
	s_waitcnt lgkmcnt(0)
	global_store_dwordx4 v[2:3], v[14:17], off sc1
	global_store_dwordx4 v[0:1], v[10:13], off sc1
	s_barrier
	s_waitcnt vmcnt(0)
	s_endpgm

.LBB3_74:
	s_waitcnt lgkmcnt(0)
	s_barrier
	s_lshl_b32 s0, s33, 19
	v_add_u32_e32 v14, s96, v16
	v_lshlrev_b32_e32 v0, 4, v16
	s_add_u32 s0, s66, s0
	v_and_b32_e32 v0, 0xf0, v0
	v_ashrrev_i32_e32 v4, 4, v14
	s_addc_u32 s1, s67, 0
	v_add_u32_e32 v15, s78, v0
	v_mov_b32_e32 v1, 0
	v_ashrrev_i32_e32 v5, 31, v4
	v_lshl_add_u64 v[8:9], s[0:1], 0, v[0:1]
	v_lshl_add_u32 v0, v4, 8, v15
	v_lshlrev_b64 v[4:5], 12, v[4:5]
	v_lshl_add_u64 v[10:11], v[8:9], 0, v[4:5]
	v_add_u32_e32 v4, 0x200, v14
	ds_read_b128 v[0:3], v0
	v_ashrrev_i32_e32 v12, 4, v4
	v_lshl_add_u32 v4, v12, 8, v15
	ds_read_b128 v[4:7], v4
	v_ashrrev_i32_e32 v13, 31, v12
	s_waitcnt lgkmcnt(1)
	global_store_dwordx4 v[10:11], v[0:3], off sc1
	s_nop 1
	v_lshlrev_b64 v[0:1], 12, v[12:13]
	v_lshl_add_u64 v[0:1], v[8:9], 0, v[0:1]
	s_waitcnt lgkmcnt(0)
	global_store_dwordx4 v[0:1], v[4:7], off sc1
	v_add_u32_e32 v0, 0x400, v14
	s_nop 0
	v_ashrrev_i32_e32 v4, 4, v0
	v_ashrrev_i32_e32 v5, 31, v4
	v_lshl_add_u32 v0, v4, 8, v15
	v_lshlrev_b64 v[4:5], 12, v[4:5]
	v_lshl_add_u64 v[10:11], v[8:9], 0, v[4:5]
	v_add_u32_e32 v4, 0x600, v14
	ds_read_b128 v[0:3], v0
	v_ashrrev_i32_e32 v12, 4, v4
	v_lshl_add_u32 v4, v12, 8, v15
	ds_read_b128 v[4:7], v4
	v_ashrrev_i32_e32 v13, 31, v12
	s_waitcnt lgkmcnt(1)
	global_store_dwordx4 v[10:11], v[0:3], off sc1
	s_nop 1
	v_lshlrev_b64 v[0:1], 12, v[12:13]
	v_lshl_add_u64 v[0:1], v[8:9], 0, v[0:1]
	s_waitcnt lgkmcnt(0)
	global_store_dwordx4 v[0:1], v[4:7], off sc1
	s_waitcnt vmcnt(0)
	s_endpgm
